# v049 + nt policy on the A-operand (HID) LDS-DMA loads of both down-projection K-loops
# speedup vs baseline: 1.0039x; 1.0039x over previous
; #define PG8_STAGE(bufoff, gbase, voff) do { _Pragma("unroll") for (int _i = 0; _i < 2; ++_i) \
;         __builtin_amdgcn_global_load_lds((const unsigned*)((const char*)(gbase) + (voff)[_i]), (LAS unsigned*)(lds + (bufoff) + ldsw + _i * 8192), 16, 0, 0); } while (0)
; #define PG8_LDA(dst, b, h) do { _Pragma("unroll") for (int m = 0; m < 4; ++m) _Pragma("unroll") for (int k = 0; k < 2; ++k) dst[m][k] = *(const LAS bf16x8*)(lds + PG8_SA(b, h) + ((aoff ^ (k * 64)) + m * 2048)); } while (0)
; #define PG8_LDB(dst, b, h) do { _Pragma("unroll") for (int n = 0; n < 2; ++n) _Pragma("unroll") for (int k = 0; k < 2; ++k) dst[n][k] = *(const LAS bf16x8*)(lds + PG8_SB(b, h) + ((boff ^ (k * 64)) + n * 2048)); } while (0)
; #define PG8_MMA(ai, bj, At, Bt) do { __builtin_amdgcn_s_setprio(1); _Pragma("unroll") for (int m = 0; m < 4; ++m) _Pragma("unroll") for (int n = 0; n < 2; ++n) _Pragma("unroll") for (int k = 0; k < 2; ++k) \
;         acc[ai][bj][m][n] = __builtin_amdgcn_mfma_f32_16x16x32_bf16(Bt[n][k], At[m][k], acc[ai][bj][m][n], 0, 0, 0); __builtin_amdgcn_s_setprio(0); } while (0)
; #define PG8_WAIT_V(n) asm volatile("s_waitcnt vmcnt(" #n ")" ::: "memory")
; #define PG8_WAIT_L(n) asm volatile("s_waitcnt lgkmcnt(" #n ")" ::: "memory")
; #define PG8_BAR __builtin_amdgcn_s_barrier()
; #define PG8_SCHED __builtin_amdgcn_sched_barrier(0)
;     ...
;             PG8_LDB(B0, 0, 0); PG8_LDB(B1, 0, 1); PG8_SCHED; PG8_LDA(At, 0, 0); PG8_STAGE(PG8_SA(1, 1), a1, voffA[1]);
;             PG8_WAIT_V(8); PG8_WAIT_L(0); PG8_BAR; if (do0) { PG8_MMA(0, 0, At, B0); PG8_MMA(0, 1, At, B1); } PG8_BAR; PG8_SCHED;
;             PG8_LDA(At, 0, 1); PG8_STAGE(PG8_SB(0, 0), b2, voffB); PG8_STAGE(PG8_SB(0, 1), b2 + hstep, voffB); PG8_STAGE(PG8_SA(0, 0), a2, vs[0]);
;             PG8_WAIT_V(8); PG8_WAIT_L(0); PG8_BAR; if (do1) { PG8_MMA(1, 0, At, B0); PG8_MMA(1, 1, At, B1); } PG8_BAR; PG8_SCHED;
;             PG8_LDB(B0, 1, 0); PG8_LDB(B1, 1, 1); PG8_SCHED; PG8_LDA(At, 1, 0); PG8_STAGE(PG8_SA(0, 1), a2, vs[1]);
;             PG8_WAIT_V(8); PG8_WAIT_L(0); PG8_BAR; if (do0) { PG8_MMA(0, 0, At, B0); PG8_MMA(0, 1, At, B1); } PG8_BAR; PG8_SCHED;
.LBB0_1100:
	ds_read_b128 v[150:153], v218
	ds_read_b128 v[154:157], v219
	ds_read_b128 v[158:161], v220
	ds_read_b128 v[162:165], v221
	ds_read_b128 v[134:137], v222
	ds_read_b128 v[138:141], v223
	ds_read_b128 v[142:145], v224
	ds_read_b128 v[146:149], v225
	v_lshl_add_u64 v[4:5], s[22:23], 0, v[212:213]
	s_add_i32 m0, s28, 0xc000
	s_waitcnt lgkmcnt(0)
	ds_read_b128 v[190:193], v226
	ds_read_b128 v[178:181], v226 offset:2048
	ds_read_b128 v[194:197], v227
	ds_read_b128 v[182:185], v227 offset:2048
	ds_read_b128 v[174:177], v226 offset:4096
	ds_read_b128 v[166:169], v226 offset:6144
	ds_read_b128 v[186:189], v227 offset:4096
	ds_read_b128 v[170:173], v227 offset:6144
	global_load_lds_dwordx4 v[4:5], off nt
	v_lshl_add_u64 v[4:5], s[22:23], 0, v[214:215]
	s_add_i32 m0, s28, 0xe000
	v_cmp_ne_u32_e64 s[6:7], 1, v228
	global_load_lds_dwordx4 v[4:5], off nt
	s_waitcnt vmcnt(8)
	s_waitcnt lgkmcnt(0)
	s_andn2_b64 vcc, exec, s[20:21]
	s_barrier
	s_cbranch_vccnz .LBB0_1102
	s_setprio 1
	v_mfma_f32_16x16x32_bf16 v[66:69], v[150:153], v[190:193], v[66:69]
	v_mfma_f32_16x16x32_bf16 v[62:65], v[158:161], v[190:193], v[62:65]
	v_mfma_f32_16x16x32_bf16 v[50:53], v[150:153], v[178:181], v[50:53]
	v_mfma_f32_16x16x32_bf16 v[46:49], v[158:161], v[178:181], v[46:49]
	v_mfma_f32_16x16x32_bf16 v[34:37], v[150:153], v[174:177], v[34:37]
	v_mfma_f32_16x16x32_bf16 v[30:33], v[158:161], v[174:177], v[30:33]
	v_mfma_f32_16x16x32_bf16 v[18:21], v[150:153], v[166:169], v[18:21]
	v_mfma_f32_16x16x32_bf16 v[14:17], v[158:161], v[166:169], v[14:17]
	v_mfma_f32_16x16x32_bf16 v[66:69], v[154:157], v[194:197], v[66:69]
	v_mfma_f32_16x16x32_bf16 v[62:65], v[162:165], v[194:197], v[62:65]
	v_mfma_f32_16x16x32_bf16 v[50:53], v[154:157], v[182:185], v[50:53]
	v_mfma_f32_16x16x32_bf16 v[46:49], v[162:165], v[182:185], v[46:49]
	v_mfma_f32_16x16x32_bf16 v[34:37], v[154:157], v[186:189], v[34:37]
	v_mfma_f32_16x16x32_bf16 v[30:33], v[162:165], v[186:189], v[30:33]
	v_mfma_f32_16x16x32_bf16 v[18:21], v[154:157], v[170:173], v[18:21]
	v_mfma_f32_16x16x32_bf16 v[14:17], v[162:165], v[170:173], v[14:17]
	v_mfma_f32_16x16x32_bf16 v[58:61], v[134:137], v[190:193], v[58:61]
	v_mfma_f32_16x16x32_bf16 v[54:57], v[142:145], v[190:193], v[54:57]
	v_mfma_f32_16x16x32_bf16 v[42:45], v[134:137], v[178:181], v[42:45]
	v_mfma_f32_16x16x32_bf16 v[38:41], v[142:145], v[178:181], v[38:41]
	v_mfma_f32_16x16x32_bf16 v[26:29], v[134:137], v[174:177], v[26:29]
	v_mfma_f32_16x16x32_bf16 v[22:25], v[142:145], v[174:177], v[22:25]
	v_mfma_f32_16x16x32_bf16 v[10:13], v[134:137], v[166:169], v[10:13]
	v_mfma_f32_16x16x32_bf16 v[4:7], v[142:145], v[166:169], v[6:9]
	v_mfma_f32_16x16x32_bf16 v[58:61], v[138:141], v[194:197], v[58:61]
	v_mfma_f32_16x16x32_bf16 v[54:57], v[146:149], v[194:197], v[54:57]
	v_mfma_f32_16x16x32_bf16 v[42:45], v[138:141], v[182:185], v[42:45]
	v_mfma_f32_16x16x32_bf16 v[38:41], v[146:149], v[182:185], v[38:41]
	v_mfma_f32_16x16x32_bf16 v[26:29], v[138:141], v[186:189], v[26:29]
	v_mfma_f32_16x16x32_bf16 v[22:25], v[146:149], v[186:189], v[22:25]
	v_mfma_f32_16x16x32_bf16 v[10:13], v[138:141], v[170:173], v[10:13]
	v_mfma_f32_16x16x32_bf16 v[6:9], v[146:149], v[170:173], v[4:7]
	s_setprio 0
.LBB0_1102:
	s_add_u32 s8, s22, 0x4000
	s_addc_u32 s9, s23, 0
	s_cmp_eq_u32 s61, s59
	s_cselect_b32 s27, s15, s9
	s_cselect_b32 s26, s14, s8
	s_cselect_b32 s25, s17, s63
	s_cselect_b32 s24, s16, s62
	s_barrier
	s_mov_b32 m0, s29
	v_lshl_add_u64 v[4:5], s[24:25], 0, v[208:209]
	s_add_u32 s8, s24, 0xb0000
	s_waitcnt lgkmcnt(0)
	ds_read_b128 v[190:193], v226 offset:16384
	ds_read_b128 v[178:181], v226 offset:18432
	ds_read_b128 v[194:197], v227 offset:16384
	ds_read_b128 v[182:185], v227 offset:18432
	ds_read_b128 v[174:177], v226 offset:20480
	ds_read_b128 v[166:169], v226 offset:22528
	ds_read_b128 v[186:189], v227 offset:20480
	ds_read_b128 v[170:173], v227 offset:22528
	global_load_lds_dwordx4 v[4:5], off
	v_lshl_add_u64 v[4:5], s[24:25], 0, v[210:211]
	s_mov_b32 m0, s30
	s_addc_u32 s9, s25, 0
	global_load_lds_dwordx4 v[4:5], off
	v_lshl_add_u64 v[4:5], s[8:9], 0, v[208:209]
	s_mov_b32 m0, s31
	v_cndmask_b32_e64 v3, 0, 1, s[18:19]
	global_load_lds_dwordx4 v[4:5], off
	v_lshl_add_u64 v[4:5], s[8:9], 0, v[210:211]
	s_mov_b32 m0, s34
	v_cmp_ne_u32_e64 s[8:9], 1, v3
	global_load_lds_dwordx4 v[4:5], off
	v_lshl_add_u64 v[4:5], s[26:27], 0, v[200:201]
	s_mov_b32 m0, s28
	s_andn2_b64 vcc, exec, s[18:19]
	global_load_lds_dwordx4 v[4:5], off nt
	v_lshl_add_u64 v[4:5], s[26:27], 0, v[202:203]
	s_mov_b32 m0, s35
	s_nop 0
	global_load_lds_dwordx4 v[4:5], off nt
	s_waitcnt vmcnt(8)
	s_waitcnt lgkmcnt(0)
	s_barrier
	s_cbranch_vccnz .LBB0_1104
	s_setprio 1
	v_mfma_f32_16x16x32_bf16 v[130:133], v[150:153], v[190:193], v[130:133]
	v_mfma_f32_16x16x32_bf16 v[126:129], v[158:161], v[190:193], v[126:129]
	v_mfma_f32_16x16x32_bf16 v[114:117], v[150:153], v[178:181], v[114:117]
	v_mfma_f32_16x16x32_bf16 v[110:113], v[158:161], v[178:181], v[110:113]
	v_mfma_f32_16x16x32_bf16 v[98:101], v[150:153], v[174:177], v[98:101]
	v_mfma_f32_16x16x32_bf16 v[94:97], v[158:161], v[174:177], v[94:97]
	v_mfma_f32_16x16x32_bf16 v[82:85], v[150:153], v[166:169], v[82:85]
	v_mfma_f32_16x16x32_bf16 v[78:81], v[158:161], v[166:169], v[78:81]
	v_mfma_f32_16x16x32_bf16 v[130:133], v[154:157], v[194:197], v[130:133]
	v_mfma_f32_16x16x32_bf16 v[126:129], v[162:165], v[194:197], v[126:129]
	v_mfma_f32_16x16x32_bf16 v[114:117], v[154:157], v[182:185], v[114:117]
	v_mfma_f32_16x16x32_bf16 v[110:113], v[162:165], v[182:185], v[110:113]
	v_mfma_f32_16x16x32_bf16 v[98:101], v[154:157], v[186:189], v[98:101]
	v_mfma_f32_16x16x32_bf16 v[94:97], v[162:165], v[186:189], v[94:97]
	v_mfma_f32_16x16x32_bf16 v[82:85], v[154:157], v[170:173], v[82:85]
	v_mfma_f32_16x16x32_bf16 v[78:81], v[162:165], v[170:173], v[78:81]
	v_mfma_f32_16x16x32_bf16 v[122:125], v[134:137], v[190:193], v[122:125]
	v_mfma_f32_16x16x32_bf16 v[118:121], v[142:145], v[190:193], v[118:121]
	v_mfma_f32_16x16x32_bf16 v[106:109], v[134:137], v[178:181], v[106:109]
	v_mfma_f32_16x16x32_bf16 v[102:105], v[142:145], v[178:181], v[102:105]
	v_mfma_f32_16x16x32_bf16 v[90:93], v[134:137], v[174:177], v[90:93]
	v_mfma_f32_16x16x32_bf16 v[86:89], v[142:145], v[174:177], v[86:89]
	v_mfma_f32_16x16x32_bf16 v[74:77], v[134:137], v[166:169], v[74:77]
	v_mfma_f32_16x16x32_bf16 v[70:73], v[142:145], v[166:169], v[70:73]
	v_mfma_f32_16x16x32_bf16 v[122:125], v[138:141], v[194:197], v[122:125]
	v_mfma_f32_16x16x32_bf16 v[118:121], v[146:149], v[194:197], v[118:121]
	v_mfma_f32_16x16x32_bf16 v[106:109], v[138:141], v[182:185], v[106:109]
	v_mfma_f32_16x16x32_bf16 v[102:105], v[146:149], v[182:185], v[102:105]
	v_mfma_f32_16x16x32_bf16 v[90:93], v[138:141], v[186:189], v[90:93]
	v_mfma_f32_16x16x32_bf16 v[86:89], v[146:149], v[186:189], v[86:89]
	v_mfma_f32_16x16x32_bf16 v[74:77], v[138:141], v[170:173], v[74:77]
	v_mfma_f32_16x16x32_bf16 v[70:73], v[146:149], v[170:173], v[70:73]
	s_setprio 0
; #define PG8_STAGE(bufoff, gbase, voff) do { _Pragma("unroll") for (int _i = 0; _i < 2; ++_i) \
;         __builtin_amdgcn_global_load_lds((const unsigned*)((const char*)(gbase) + (voff)[_i]), (LAS unsigned*)(lds + (bufoff) + ldsw + _i * 8192), 16, 0, 0); } while (0)
; #define PG8_LDA(dst, b, h) do { _Pragma("unroll") for (int m = 0; m < 4; ++m) _Pragma("unroll") for (int k = 0; k < 2; ++k) dst[m][k] = *(const LAS bf16x8*)(lds + PG8_SA(b, h) + ((aoff ^ (k * 64)) + m * 2048)); } while (0)
; #define PG8_LDB(dst, b, h) do { _Pragma("unroll") for (int n = 0; n < 2; ++n) _Pragma("unroll") for (int k = 0; k < 2; ++k) dst[n][k] = *(const LAS bf16x8*)(lds + PG8_SB(b, h) + ((boff ^ (k * 64)) + n * 2048)); } while (0)
; #define PG8_MMA(ai, bj, At, Bt) do { __builtin_amdgcn_s_setprio(1); _Pragma("unroll") for (int m = 0; m < 4; ++m) _Pragma("unroll") for (int n = 0; n < 2; ++n) _Pragma("unroll") for (int k = 0; k < 2; ++k) \
;         acc[ai][bj][m][n] = __builtin_amdgcn_mfma_f32_16x16x32_bf16(Bt[n][k], At[m][k], acc[ai][bj][m][n], 0, 0, 0); __builtin_amdgcn_s_setprio(0); } while (0)
; #define PG8_WAIT_V(n) asm volatile("s_waitcnt vmcnt(" #n ")" ::: "memory")
; #define PG8_WAIT_L(n) asm volatile("s_waitcnt lgkmcnt(" #n ")" ::: "memory")
; #define PG8_BAR __builtin_amdgcn_s_barrier()
; #define PG8_SCHED __builtin_amdgcn_sched_barrier(0)
;     ...
;             PG8_LDB(B0, 1, 0); PG8_LDB(B1, 1, 1); PG8_SCHED; PG8_LDA(At, 1, 0); PG8_STAGE(PG8_SA(0, 1), a2, vs[1]);
;             PG8_WAIT_V(8); PG8_WAIT_L(0); PG8_BAR; if (do0) { PG8_MMA(0, 0, At, B0); PG8_MMA(0, 1, At, B1); } PG8_BAR; PG8_SCHED;
.LBB0_1104:
	s_barrier
	s_add_i32 s64, 0, 0x18000
	v_add_u32_e32 v3, s64, v199
	v_add_u32_e32 v4, s64, v216
	ds_read_b128 v[150:153], v3
	ds_read_b128 v[154:157], v4
	v_add_u32_e32 v3, s48, v199
	s_add_i32 s64, 0, 0x1c000
	v_add_u32_e32 v4, s48, v216
	ds_read_b128 v[158:161], v3
	ds_read_b128 v[162:165], v4
	v_add_u32_e32 v3, s64, v199
	v_add_u32_e32 v4, s64, v216
	ds_read_b128 v[134:137], v3
	ds_read_b128 v[138:141], v4
	v_add_u32_e32 v3, s49, v199
	v_add_u32_e32 v4, s49, v216
	ds_read_b128 v[142:145], v3
	ds_read_b128 v[146:149], v4
	s_mov_b32 m0, s36
	v_lshl_add_u64 v[4:5], s[26:27], 0, v[204:205]
	s_waitcnt lgkmcnt(0)
	ds_read_b128 v[190:193], v226 offset:32768
	ds_read_b128 v[178:181], v226 offset:34816
	ds_read_b128 v[194:197], v227 offset:32768
	ds_read_b128 v[182:185], v227 offset:34816
	ds_read_b128 v[174:177], v226 offset:36864
	ds_read_b128 v[166:169], v226 offset:38912
	ds_read_b128 v[186:189], v227 offset:36864
	ds_read_b128 v[170:173], v227 offset:38912
	global_load_lds_dwordx4 v[4:5], off nt
	v_lshl_add_u64 v[4:5], s[26:27], 0, v[206:207]
	s_mov_b32 m0, s37
	s_and_b64 vcc, exec, s[6:7]
	global_load_lds_dwordx4 v[4:5], off nt
	s_waitcnt vmcnt(8)
	s_waitcnt lgkmcnt(0)
	s_barrier
	s_cbranch_vccnz .LBB0_1106
	s_setprio 1
	v_mfma_f32_16x16x32_bf16 v[66:69], v[150:153], v[190:193], v[66:69]
	v_mfma_f32_16x16x32_bf16 v[62:65], v[158:161], v[190:193], v[62:65]
	v_mfma_f32_16x16x32_bf16 v[50:53], v[150:153], v[178:181], v[50:53]
	v_mfma_f32_16x16x32_bf16 v[46:49], v[158:161], v[178:181], v[46:49]
	v_mfma_f32_16x16x32_bf16 v[34:37], v[150:153], v[174:177], v[34:37]
	v_mfma_f32_16x16x32_bf16 v[30:33], v[158:161], v[174:177], v[30:33]
	v_mfma_f32_16x16x32_bf16 v[18:21], v[150:153], v[166:169], v[18:21]
	v_mfma_f32_16x16x32_bf16 v[14:17], v[158:161], v[166:169], v[14:17]
	v_mfma_f32_16x16x32_bf16 v[66:69], v[154:157], v[194:197], v[66:69]
	v_mfma_f32_16x16x32_bf16 v[62:65], v[162:165], v[194:197], v[62:65]
	v_mfma_f32_16x16x32_bf16 v[50:53], v[154:157], v[182:185], v[50:53]
	v_mfma_f32_16x16x32_bf16 v[46:49], v[162:165], v[182:185], v[46:49]
	v_mfma_f32_16x16x32_bf16 v[34:37], v[154:157], v[186:189], v[34:37]
	v_mfma_f32_16x16x32_bf16 v[30:33], v[162:165], v[186:189], v[30:33]
	v_mfma_f32_16x16x32_bf16 v[18:21], v[154:157], v[170:173], v[18:21]
	v_mfma_f32_16x16x32_bf16 v[14:17], v[162:165], v[170:173], v[14:17]
	v_mfma_f32_16x16x32_bf16 v[58:61], v[134:137], v[190:193], v[58:61]
	v_mfma_f32_16x16x32_bf16 v[54:57], v[142:145], v[190:193], v[54:57]
	v_mfma_f32_16x16x32_bf16 v[42:45], v[134:137], v[178:181], v[42:45]
	v_mfma_f32_16x16x32_bf16 v[38:41], v[142:145], v[178:181], v[38:41]
	v_mfma_f32_16x16x32_bf16 v[26:29], v[134:137], v[174:177], v[26:29]
	v_mfma_f32_16x16x32_bf16 v[22:25], v[142:145], v[174:177], v[22:25]
	v_mfma_f32_16x16x32_bf16 v[10:13], v[134:137], v[166:169], v[10:13]
	v_mfma_f32_16x16x32_bf16 v[4:7], v[142:145], v[166:169], v[6:9]
	v_mfma_f32_16x16x32_bf16 v[58:61], v[138:141], v[194:197], v[58:61]
	v_mfma_f32_16x16x32_bf16 v[54:57], v[146:149], v[194:197], v[54:57]
	v_mfma_f32_16x16x32_bf16 v[42:45], v[138:141], v[182:185], v[42:45]
	v_mfma_f32_16x16x32_bf16 v[38:41], v[146:149], v[182:185], v[38:41]
	v_mfma_f32_16x16x32_bf16 v[26:29], v[138:141], v[186:189], v[26:29]
	v_mfma_f32_16x16x32_bf16 v[22:25], v[146:149], v[186:189], v[22:25]
	v_mfma_f32_16x16x32_bf16 v[10:13], v[138:141], v[170:173], v[10:13]
	v_mfma_f32_16x16x32_bf16 v[6:9], v[146:149], v[170:173], v[4:7]
	s_setprio 0
; #define PG8_STAGE(bufoff, gbase, voff) do { _Pragma("unroll") for (int _i = 0; _i < 2; ++_i) \
;         __builtin_amdgcn_global_load_lds((const unsigned*)((const char*)(gbase) + (voff)[_i]), (LAS unsigned*)(lds + (bufoff) + ldsw + _i * 8192), 16, 0, 0); } while (0)
; #define PG8_LDA(dst, b, h) do { _Pragma("unroll") for (int m = 0; m < 4; ++m) _Pragma("unroll") for (int k = 0; k < 2; ++k) dst[m][k] = *(const LAS bf16x8*)(lds + PG8_SA(b, h) + ((aoff ^ (k * 64)) + m * 2048)); } while (0)
; #define PG8_MMA(ai, bj, At, Bt) do { __builtin_amdgcn_s_setprio(1); _Pragma("unroll") for (int m = 0; m < 4; ++m) _Pragma("unroll") for (int n = 0; n < 2; ++n) _Pragma("unroll") for (int k = 0; k < 2; ++k) \
;         acc[ai][bj][m][n] = __builtin_amdgcn_mfma_f32_16x16x32_bf16(Bt[n][k], At[m][k], acc[ai][bj][m][n], 0, 0, 0); __builtin_amdgcn_s_setprio(0); } while (0)
; #define PG8_WAIT_V(n) asm volatile("s_waitcnt vmcnt(" #n ")" ::: "memory")
; #define PG8_WAIT_L(n) asm volatile("s_waitcnt lgkmcnt(" #n ")" ::: "memory")
; #define PG8_BAR __builtin_amdgcn_s_barrier()
; #define PG8_SCHED __builtin_amdgcn_sched_barrier(0)
;     ...
;             PG8_LDA(At, 1, 1); PG8_STAGE(PG8_SB(1, 0), b3, voffB); PG8_STAGE(PG8_SB(1, 1), b3 + hstep, voffB); PG8_STAGE(PG8_SA(1, 0), a3, vs[0]);
;             PG8_WAIT_V(8); PG8_WAIT_L(0); PG8_BAR; if (do1) { PG8_MMA(1, 0, At, B0); PG8_MMA(1, 1, At, B1); } PG8_BAR; PG8_SCHED;
.LBB0_1106:
	s_add_u32 s6, s26, 0x4000
	s_addc_u32 s7, s27, 0
	s_add_u32 s26, s24, 0x4000
	s_addc_u32 s27, s25, 0
	s_barrier
	s_mov_b32 m0, s39
	v_lshl_add_u64 v[4:5], s[26:27], 0, v[208:209]
	s_add_u32 s24, s24, 0xb4000
	s_waitcnt lgkmcnt(0)
	ds_read_b128 v[190:193], v226 offset:49152
	ds_read_b128 v[178:181], v226 offset:51200
	ds_read_b128 v[194:197], v227 offset:49152
	ds_read_b128 v[182:185], v227 offset:51200
	ds_read_b128 v[174:177], v226 offset:53248
	ds_read_b128 v[166:169], v226 offset:55296
	ds_read_b128 v[186:189], v227 offset:53248
	ds_read_b128 v[170:173], v227 offset:55296
	global_load_lds_dwordx4 v[4:5], off
	v_lshl_add_u64 v[4:5], s[26:27], 0, v[210:211]
	s_mov_b32 m0, s40
	s_addc_u32 s25, s25, 0
	global_load_lds_dwordx4 v[4:5], off
	v_lshl_add_u64 v[4:5], s[24:25], 0, v[208:209]
	s_mov_b32 m0, s43
	s_and_b64 vcc, exec, s[8:9]
	global_load_lds_dwordx4 v[4:5], off
	v_lshl_add_u64 v[4:5], s[24:25], 0, v[210:211]
	s_mov_b32 m0, s44
	s_nop 0
	global_load_lds_dwordx4 v[4:5], off
	v_lshl_add_u64 v[4:5], s[6:7], 0, v[200:201]
	s_mov_b32 m0, s41
	s_nop 0
	global_load_lds_dwordx4 v[4:5], off nt
	v_lshl_add_u64 v[4:5], s[6:7], 0, v[202:203]
	s_mov_b32 m0, s42
	s_nop 0
	global_load_lds_dwordx4 v[4:5], off nt
	s_waitcnt vmcnt(8)
	s_waitcnt lgkmcnt(0)
	s_barrier
	s_cbranch_vccnz .LBB0_1099
	s_setprio 1
	v_mfma_f32_16x16x32_bf16 v[130:133], v[150:153], v[190:193], v[130:133]
	v_mfma_f32_16x16x32_bf16 v[126:129], v[158:161], v[190:193], v[126:129]
	v_mfma_f32_16x16x32_bf16 v[114:117], v[150:153], v[178:181], v[114:117]
	v_mfma_f32_16x16x32_bf16 v[110:113], v[158:161], v[178:181], v[110:113]
	v_mfma_f32_16x16x32_bf16 v[98:101], v[150:153], v[174:177], v[98:101]
	v_mfma_f32_16x16x32_bf16 v[94:97], v[158:161], v[174:177], v[94:97]
	v_mfma_f32_16x16x32_bf16 v[82:85], v[150:153], v[166:169], v[82:85]
	v_mfma_f32_16x16x32_bf16 v[78:81], v[158:161], v[166:169], v[78:81]
	v_mfma_f32_16x16x32_bf16 v[130:133], v[154:157], v[194:197], v[130:133]
	v_mfma_f32_16x16x32_bf16 v[126:129], v[162:165], v[194:197], v[126:129]
	v_mfma_f32_16x16x32_bf16 v[114:117], v[154:157], v[182:185], v[114:117]
	v_mfma_f32_16x16x32_bf16 v[110:113], v[162:165], v[182:185], v[110:113]
	v_mfma_f32_16x16x32_bf16 v[98:101], v[154:157], v[186:189], v[98:101]
	v_mfma_f32_16x16x32_bf16 v[94:97], v[162:165], v[186:189], v[94:97]
	v_mfma_f32_16x16x32_bf16 v[82:85], v[154:157], v[170:173], v[82:85]
	v_mfma_f32_16x16x32_bf16 v[78:81], v[162:165], v[170:173], v[78:81]
	v_mfma_f32_16x16x32_bf16 v[122:125], v[134:137], v[190:193], v[122:125]
	v_mfma_f32_16x16x32_bf16 v[118:121], v[142:145], v[190:193], v[118:121]
	v_mfma_f32_16x16x32_bf16 v[106:109], v[134:137], v[178:181], v[106:109]
	v_mfma_f32_16x16x32_bf16 v[102:105], v[142:145], v[178:181], v[102:105]
	v_mfma_f32_16x16x32_bf16 v[90:93], v[134:137], v[174:177], v[90:93]
	v_mfma_f32_16x16x32_bf16 v[86:89], v[142:145], v[174:177], v[86:89]
	v_mfma_f32_16x16x32_bf16 v[74:77], v[134:137], v[166:169], v[74:77]
	v_mfma_f32_16x16x32_bf16 v[70:73], v[142:145], v[166:169], v[70:73]
	v_mfma_f32_16x16x32_bf16 v[122:125], v[138:141], v[194:197], v[122:125]
	v_mfma_f32_16x16x32_bf16 v[118:121], v[146:149], v[194:197], v[118:121]
	v_mfma_f32_16x16x32_bf16 v[106:109], v[138:141], v[182:185], v[106:109]
	v_mfma_f32_16x16x32_bf16 v[102:105], v[146:149], v[182:185], v[102:105]
	v_mfma_f32_16x16x32_bf16 v[90:93], v[138:141], v[186:189], v[90:93]
	v_mfma_f32_16x16x32_bf16 v[86:89], v[146:149], v[186:189], v[86:89]
	v_mfma_f32_16x16x32_bf16 v[74:77], v[138:141], v[170:173], v[74:77]
	v_mfma_f32_16x16x32_bf16 v[70:73], v[146:149], v[170:173], v[70:73]
	s_setprio 0
	s_branch .LBB0_1099

; #define PG8_STAGE(bufoff, gbase, voff) do { _Pragma("unroll") for (int _i = 0; _i < 2; ++_i) \
;         __builtin_amdgcn_global_load_lds((const unsigned*)((const char*)(gbase) + (voff)[_i]), (LAS unsigned*)(lds + (bufoff) + ldsw + _i * 8192), 16, 0, 0); } while (0)
; #define PG8_LDA(dst, b, h) do { _Pragma("unroll") for (int m = 0; m < 4; ++m) _Pragma("unroll") for (int k = 0; k < 2; ++k) dst[m][k] = *(const LAS bf16x8*)(lds + PG8_SA(b, h) + ((aoff ^ (k * 64)) + m * 2048)); } while (0)
; #define PG8_LDB(dst, b, h) do { _Pragma("unroll") for (int n = 0; n < 2; ++n) _Pragma("unroll") for (int k = 0; k < 2; ++k) dst[n][k] = *(const LAS bf16x8*)(lds + PG8_SB(b, h) + ((boff ^ (k * 64)) + n * 2048)); } while (0)
; #define PG8_MMA(ai, bj, At, Bt) do { __builtin_amdgcn_s_setprio(1); _Pragma("unroll") for (int m = 0; m < 4; ++m) _Pragma("unroll") for (int n = 0; n < 2; ++n) _Pragma("unroll") for (int k = 0; k < 2; ++k) \
;         acc[ai][bj][m][n] = __builtin_amdgcn_mfma_f32_16x16x32_bf16(Bt[n][k], At[m][k], acc[ai][bj][m][n], 0, 0, 0); __builtin_amdgcn_s_setprio(0); } while (0)
; #define PG8_WAIT_V(n) asm volatile("s_waitcnt vmcnt(" #n ")" ::: "memory")
; #define PG8_WAIT_L(n) asm volatile("s_waitcnt lgkmcnt(" #n ")" ::: "memory")
; #define PG8_BAR __builtin_amdgcn_s_barrier()
; #define PG8_SCHED __builtin_amdgcn_sched_barrier(0)
;     ...
;             PG8_LDB(B0, 0, 0); PG8_LDB(B1, 0, 1); PG8_SCHED; PG8_LDA(At, 0, 0); PG8_STAGE(PG8_SA(1, 1), a1, voffA[1]);
;             PG8_WAIT_V(8); PG8_WAIT_L(0); PG8_BAR; if (do0) { PG8_MMA(0, 0, At, B0); PG8_MMA(0, 1, At, B1); } PG8_BAR; PG8_SCHED;
;             PG8_LDA(At, 0, 1); PG8_STAGE(PG8_SB(0, 0), b2, voffB); PG8_STAGE(PG8_SB(0, 1), b2 + hstep, voffB); PG8_STAGE(PG8_SA(0, 0), a2, vs[0]);
;             PG8_WAIT_V(8); PG8_WAIT_L(0); PG8_BAR; if (do1) { PG8_MMA(1, 0, At, B0); PG8_MMA(1, 1, At, B1); } PG8_BAR; PG8_SCHED;
;             PG8_LDB(B0, 1, 0); PG8_LDB(B1, 1, 1); PG8_SCHED; PG8_LDA(At, 1, 0); PG8_STAGE(PG8_SA(0, 1), a2, vs[1]);
;             PG8_WAIT_V(8); PG8_WAIT_L(0); PG8_BAR; if (do0) { PG8_MMA(0, 0, At, B0); PG8_MMA(0, 1, At, B1); } PG8_BAR; PG8_SCHED;
.LBB0_2411:
	ds_read_b128 v[146:149], v153
	ds_read_b128 v[168:171], v154
	ds_read_b128 v[172:175], v155
	ds_read_b128 v[176:179], v156
	ds_read_b128 v[180:183], v157
	ds_read_b128 v[184:187], v158
	ds_read_b128 v[188:191], v159
	ds_read_b128 v[192:195], v160
	s_add_u32 s20, s18, 0x4000
	s_addc_u32 s21, s19, 0
	s_cmp_eq_u32 s56, 40
	s_cselect_b32 s26, s14, s20
	s_cselect_b32 s27, s15, s21
	s_cselect_b32 s22, s16, s54
	s_cselect_b32 s23, s17, s55
	s_add_u32 s20, s26, 0x4000
	s_addc_u32 s21, s27, 0
	v_lshl_add_u64 v[196:197], s[18:19], 0, v[142:143]
	s_add_i32 m0, s34, 0xc000
	ds_read_b128 v[200:203], v161
	ds_read_b128 v[204:207], v161 offset:2048
	ds_read_b128 v[208:211], v162
	ds_read_b128 v[212:215], v162 offset:2048
	ds_read_b128 v[216:219], v161 offset:4096
	ds_read_b128 v[220:223], v161 offset:6144
	ds_read_b128 v[224:227], v162 offset:4096
	ds_read_b128 v[228:231], v162 offset:6144
	global_load_lds_dwordx4 v[196:197], off nt
	v_lshl_add_u64 v[196:197], s[18:19], 0, v[144:145]
	s_add_i32 m0, s34, 0xe000
	s_add_u32 s24, s22, 0x4000
	global_load_lds_dwordx4 v[196:197], off nt
	s_waitcnt vmcnt(8)
	s_waitcnt lgkmcnt(0)
	s_addc_u32 s25, s23, 0
	s_barrier
	s_setprio 1
	v_mfma_f32_16x16x32_bf16 v[126:129], v[146:149], v[200:203], v[126:129]
	v_mfma_f32_16x16x32_bf16 v[122:125], v[172:175], v[200:203], v[122:125]
	v_mfma_f32_16x16x32_bf16 v[114:117], v[146:149], v[204:207], v[114:117]
	v_mfma_f32_16x16x32_bf16 v[106:109], v[172:175], v[204:207], v[106:109]
	v_mfma_f32_16x16x32_bf16 v[98:101], v[146:149], v[216:219], v[98:101]
	v_mfma_f32_16x16x32_bf16 v[90:93], v[172:175], v[216:219], v[90:93]
	v_mfma_f32_16x16x32_bf16 v[82:85], v[146:149], v[220:223], v[82:85]
	v_mfma_f32_16x16x32_bf16 v[74:77], v[172:175], v[220:223], v[74:77]
	v_mfma_f32_16x16x32_bf16 v[126:129], v[168:171], v[208:211], v[126:129]
	v_mfma_f32_16x16x32_bf16 v[122:125], v[176:179], v[208:211], v[122:125]
	v_mfma_f32_16x16x32_bf16 v[114:117], v[168:171], v[212:215], v[114:117]
	v_mfma_f32_16x16x32_bf16 v[106:109], v[176:179], v[212:215], v[106:109]
	v_mfma_f32_16x16x32_bf16 v[98:101], v[168:171], v[224:227], v[98:101]
	v_mfma_f32_16x16x32_bf16 v[90:93], v[176:179], v[224:227], v[90:93]
	v_mfma_f32_16x16x32_bf16 v[82:85], v[168:171], v[228:231], v[82:85]
	v_mfma_f32_16x16x32_bf16 v[74:77], v[176:179], v[228:231], v[74:77]
	v_mfma_f32_16x16x32_bf16 v[118:121], v[180:183], v[200:203], v[118:121]
	v_mfma_f32_16x16x32_bf16 v[110:113], v[188:191], v[200:203], v[110:113]
	v_mfma_f32_16x16x32_bf16 v[102:105], v[180:183], v[204:207], v[102:105]
	v_mfma_f32_16x16x32_bf16 v[94:97], v[188:191], v[204:207], v[94:97]
	v_mfma_f32_16x16x32_bf16 v[86:89], v[180:183], v[216:219], v[86:89]
	v_mfma_f32_16x16x32_bf16 v[78:81], v[188:191], v[216:219], v[78:81]
	v_mfma_f32_16x16x32_bf16 v[70:73], v[180:183], v[220:223], v[70:73]
	v_mfma_f32_16x16x32_bf16 v[66:69], v[188:191], v[220:223], v[66:69]
	v_mfma_f32_16x16x32_bf16 v[118:121], v[184:187], v[208:211], v[118:121]
	v_mfma_f32_16x16x32_bf16 v[110:113], v[192:195], v[208:211], v[110:113]
	v_mfma_f32_16x16x32_bf16 v[102:105], v[184:187], v[212:215], v[102:105]
	v_mfma_f32_16x16x32_bf16 v[94:97], v[192:195], v[212:215], v[94:97]
	v_mfma_f32_16x16x32_bf16 v[86:89], v[184:187], v[224:227], v[86:89]
	v_mfma_f32_16x16x32_bf16 v[78:81], v[192:195], v[224:227], v[78:81]
	v_mfma_f32_16x16x32_bf16 v[70:73], v[184:187], v[228:231], v[70:73]
	v_mfma_f32_16x16x32_bf16 v[66:69], v[192:195], v[228:231], v[66:69]
	s_setprio 0
	s_barrier
	s_add_i32 s57, s42, s30
	v_lshl_add_u64 v[196:197], s[22:23], 0, v[132:133]
	s_mov_b32 m0, s57
	ds_read_b128 v[200:203], v161 offset:16384
	ds_read_b128 v[204:207], v161 offset:18432
	ds_read_b128 v[208:211], v162 offset:16384
	ds_read_b128 v[212:215], v162 offset:18432
	ds_read_b128 v[216:219], v161 offset:20480
	ds_read_b128 v[220:223], v161 offset:22528
	ds_read_b128 v[224:227], v162 offset:20480
	ds_read_b128 v[228:231], v162 offset:22528
	global_load_lds_dwordx4 v[196:197], off
	s_add_i32 m0, s57, 0x2000
	s_add_u32 s58, s22, 0xb0000
	v_lshl_add_u64 v[196:197], s[22:23], 0, v[130:131]
	s_addc_u32 s59, s23, 0
	s_add_i32 s57, s43, s30
	global_load_lds_dwordx4 v[196:197], off
	v_lshl_add_u64 v[196:197], s[58:59], 0, v[132:133]
	s_mov_b32 m0, s57
	s_nop 0
	global_load_lds_dwordx4 v[196:197], off
	v_lshl_add_u64 v[196:197], s[58:59], 0, v[130:131]
	s_add_i32 m0, s57, 0x2000
	s_nop 0
	global_load_lds_dwordx4 v[196:197], off
	v_lshl_add_u64 v[196:197], s[26:27], 0, v[134:135]
	s_mov_b32 m0, s34
	s_nop 0
	global_load_lds_dwordx4 v[196:197], off nt
	v_lshl_add_u64 v[196:197], s[26:27], 0, v[136:137]
	s_mov_b32 m0, s35
	s_nop 0
	global_load_lds_dwordx4 v[196:197], off nt
	s_waitcnt vmcnt(8)
	s_waitcnt lgkmcnt(0)
	s_barrier
; #define PG8_STAGE(bufoff, gbase, voff) do { _Pragma("unroll") for (int _i = 0; _i < 2; ++_i) \
;         __builtin_amdgcn_global_load_lds((const unsigned*)((const char*)(gbase) + (voff)[_i]), (LAS unsigned*)(lds + (bufoff) + ldsw + _i * 8192), 16, 0, 0); } while (0)
; #define PG8_LDA(dst, b, h) do { _Pragma("unroll") for (int m = 0; m < 4; ++m) _Pragma("unroll") for (int k = 0; k < 2; ++k) dst[m][k] = *(const LAS bf16x8*)(lds + PG8_SA(b, h) + ((aoff ^ (k * 64)) + m * 2048)); } while (0)
; #define PG8_LDB(dst, b, h) do { _Pragma("unroll") for (int n = 0; n < 2; ++n) _Pragma("unroll") for (int k = 0; k < 2; ++k) dst[n][k] = *(const LAS bf16x8*)(lds + PG8_SB(b, h) + ((boff ^ (k * 64)) + n * 2048)); } while (0)
; #define PG8_MMA(ai, bj, At, Bt) do { __builtin_amdgcn_s_setprio(1); _Pragma("unroll") for (int m = 0; m < 4; ++m) _Pragma("unroll") for (int n = 0; n < 2; ++n) _Pragma("unroll") for (int k = 0; k < 2; ++k) \
;         acc[ai][bj][m][n] = __builtin_amdgcn_mfma_f32_16x16x32_bf16(Bt[n][k], At[m][k], acc[ai][bj][m][n], 0, 0, 0); __builtin_amdgcn_s_setprio(0); } while (0)
; #define PG8_WAIT_V(n) asm volatile("s_waitcnt vmcnt(" #n ")" ::: "memory")
; #define PG8_WAIT_L(n) asm volatile("s_waitcnt lgkmcnt(" #n ")" ::: "memory")
; #define PG8_BAR __builtin_amdgcn_s_barrier()
; #define PG8_SCHED __builtin_amdgcn_sched_barrier(0)
;     ...
;             PG8_WAIT_V(8); PG8_WAIT_L(0); PG8_BAR; if (do1) { PG8_MMA(1, 0, At, B0); PG8_MMA(1, 1, At, B1); } PG8_BAR; PG8_SCHED;
;             PG8_LDB(B0, 1, 0); PG8_LDB(B1, 1, 1); PG8_SCHED; PG8_LDA(At, 1, 0); PG8_STAGE(PG8_SA(0, 1), a2, vs[1]);
;             PG8_WAIT_V(8); PG8_WAIT_L(0); PG8_BAR; if (do0) { PG8_MMA(0, 0, At, B0); PG8_MMA(0, 1, At, B1); } PG8_BAR; PG8_SCHED;
	s_setprio 1
	v_mfma_f32_16x16x32_bf16 v[62:65], v[146:149], v[200:203], v[62:65]
	v_mfma_f32_16x16x32_bf16 v[58:61], v[172:175], v[200:203], v[58:61]
	v_mfma_f32_16x16x32_bf16 v[46:49], v[146:149], v[204:207], v[46:49]
	v_mfma_f32_16x16x32_bf16 v[42:45], v[172:175], v[204:207], v[42:45]
	v_mfma_f32_16x16x32_bf16 v[30:33], v[146:149], v[216:219], v[30:33]
	v_mfma_f32_16x16x32_bf16 v[26:29], v[172:175], v[216:219], v[26:29]
	v_mfma_f32_16x16x32_bf16 v[14:17], v[146:149], v[220:223], v[14:17]
	v_mfma_f32_16x16x32_bf16 v[10:13], v[172:175], v[220:223], v[10:13]
	v_mfma_f32_16x16x32_bf16 v[62:65], v[168:171], v[208:211], v[62:65]
	v_mfma_f32_16x16x32_bf16 v[58:61], v[176:179], v[208:211], v[58:61]
	v_mfma_f32_16x16x32_bf16 v[46:49], v[168:171], v[212:215], v[46:49]
	v_mfma_f32_16x16x32_bf16 v[42:45], v[176:179], v[212:215], v[42:45]
	v_mfma_f32_16x16x32_bf16 v[30:33], v[168:171], v[224:227], v[30:33]
	v_mfma_f32_16x16x32_bf16 v[26:29], v[176:179], v[224:227], v[26:29]
	v_mfma_f32_16x16x32_bf16 v[14:17], v[168:171], v[228:231], v[14:17]
	v_mfma_f32_16x16x32_bf16 v[10:13], v[176:179], v[228:231], v[10:13]
	v_mfma_f32_16x16x32_bf16 v[54:57], v[180:183], v[200:203], v[54:57]
	v_mfma_f32_16x16x32_bf16 v[50:53], v[188:191], v[200:203], v[50:53]
	v_mfma_f32_16x16x32_bf16 v[38:41], v[180:183], v[204:207], v[38:41]
	v_mfma_f32_16x16x32_bf16 v[34:37], v[188:191], v[204:207], v[34:37]
	v_mfma_f32_16x16x32_bf16 v[22:25], v[180:183], v[216:219], v[22:25]
	v_mfma_f32_16x16x32_bf16 v[18:21], v[188:191], v[216:219], v[18:21]
	v_mfma_f32_16x16x32_bf16 v[6:9], v[180:183], v[220:223], v[6:9]
	v_mfma_f32_16x16x32_bf16 v[2:5], v[188:191], v[220:223], v[2:5]
	v_mfma_f32_16x16x32_bf16 v[54:57], v[184:187], v[208:211], v[54:57]
	v_mfma_f32_16x16x32_bf16 v[50:53], v[192:195], v[208:211], v[50:53]
	v_mfma_f32_16x16x32_bf16 v[38:41], v[184:187], v[212:215], v[38:41]
	v_mfma_f32_16x16x32_bf16 v[34:37], v[192:195], v[212:215], v[34:37]
	v_mfma_f32_16x16x32_bf16 v[22:25], v[184:187], v[224:227], v[22:25]
	v_mfma_f32_16x16x32_bf16 v[18:21], v[192:195], v[224:227], v[18:21]
	v_mfma_f32_16x16x32_bf16 v[6:9], v[184:187], v[228:231], v[6:9]
	v_mfma_f32_16x16x32_bf16 v[2:5], v[192:195], v[228:231], v[2:5]
	s_setprio 0
	s_barrier
	s_add_i32 s57, 0, 0x18000
	v_add_u32_e32 v146, s57, v150
	v_add_u32_e32 v167, s57, v151
	s_add_i32 s58, 0, 0x1c000
	ds_read_b128 v[146:149], v146
	ds_read_b128 v[168:171], v167
	ds_read_b128 v[172:175], v163
	ds_read_b128 v[176:179], v164
	v_add_u32_e32 v167, s58, v150
	v_add_u32_e32 v184, s58, v151
	ds_read_b128 v[180:183], v167
	ds_read_b128 v[184:187], v184
	ds_read_b128 v[188:191], v165
	ds_read_b128 v[192:195], v166
	s_mov_b32 m0, s36
	v_lshl_add_u64 v[196:197], s[26:27], 0, v[138:139]
	ds_read_b128 v[200:203], v161 offset:32768
	ds_read_b128 v[204:207], v161 offset:34816
	ds_read_b128 v[208:211], v162 offset:32768
	ds_read_b128 v[212:215], v162 offset:34816
	ds_read_b128 v[216:219], v161 offset:36864
	ds_read_b128 v[220:223], v161 offset:38912
	ds_read_b128 v[224:227], v162 offset:36864
	ds_read_b128 v[228:231], v162 offset:38912
	global_load_lds_dwordx4 v[196:197], off nt
	v_lshl_add_u64 v[196:197], s[26:27], 0, v[140:141]
	s_mov_b32 m0, s37
	s_nop 0
	global_load_lds_dwordx4 v[196:197], off nt
	s_waitcnt vmcnt(8)
	s_waitcnt lgkmcnt(0)
	s_barrier
	s_setprio 1
	v_mfma_f32_16x16x32_bf16 v[126:129], v[146:149], v[200:203], v[126:129]
	v_mfma_f32_16x16x32_bf16 v[122:125], v[172:175], v[200:203], v[122:125]
	v_mfma_f32_16x16x32_bf16 v[114:117], v[146:149], v[204:207], v[114:117]
	v_mfma_f32_16x16x32_bf16 v[106:109], v[172:175], v[204:207], v[106:109]
	v_mfma_f32_16x16x32_bf16 v[98:101], v[146:149], v[216:219], v[98:101]
	v_mfma_f32_16x16x32_bf16 v[90:93], v[172:175], v[216:219], v[90:93]
	v_mfma_f32_16x16x32_bf16 v[82:85], v[146:149], v[220:223], v[82:85]
	v_mfma_f32_16x16x32_bf16 v[74:77], v[172:175], v[220:223], v[74:77]
	v_mfma_f32_16x16x32_bf16 v[126:129], v[168:171], v[208:211], v[126:129]
	v_mfma_f32_16x16x32_bf16 v[122:125], v[176:179], v[208:211], v[122:125]
	v_mfma_f32_16x16x32_bf16 v[114:117], v[168:171], v[212:215], v[114:117]
	v_mfma_f32_16x16x32_bf16 v[106:109], v[176:179], v[212:215], v[106:109]
	v_mfma_f32_16x16x32_bf16 v[98:101], v[168:171], v[224:227], v[98:101]
	v_mfma_f32_16x16x32_bf16 v[90:93], v[176:179], v[224:227], v[90:93]
	v_mfma_f32_16x16x32_bf16 v[82:85], v[168:171], v[228:231], v[82:85]
	v_mfma_f32_16x16x32_bf16 v[74:77], v[176:179], v[228:231], v[74:77]
	v_mfma_f32_16x16x32_bf16 v[118:121], v[180:183], v[200:203], v[118:121]
	v_mfma_f32_16x16x32_bf16 v[110:113], v[188:191], v[200:203], v[110:113]
	v_mfma_f32_16x16x32_bf16 v[102:105], v[180:183], v[204:207], v[102:105]
	v_mfma_f32_16x16x32_bf16 v[94:97], v[188:191], v[204:207], v[94:97]
	v_mfma_f32_16x16x32_bf16 v[86:89], v[180:183], v[216:219], v[86:89]
	v_mfma_f32_16x16x32_bf16 v[78:81], v[188:191], v[216:219], v[78:81]
	v_mfma_f32_16x16x32_bf16 v[70:73], v[180:183], v[220:223], v[70:73]
	v_mfma_f32_16x16x32_bf16 v[66:69], v[188:191], v[220:223], v[66:69]
	v_mfma_f32_16x16x32_bf16 v[118:121], v[184:187], v[208:211], v[118:121]
	v_mfma_f32_16x16x32_bf16 v[110:113], v[192:195], v[208:211], v[110:113]
	v_mfma_f32_16x16x32_bf16 v[102:105], v[184:187], v[212:215], v[102:105]
	v_mfma_f32_16x16x32_bf16 v[94:97], v[192:195], v[212:215], v[94:97]
	v_mfma_f32_16x16x32_bf16 v[86:89], v[184:187], v[224:227], v[86:89]
	v_mfma_f32_16x16x32_bf16 v[78:81], v[192:195], v[224:227], v[78:81]
	v_mfma_f32_16x16x32_bf16 v[70:73], v[184:187], v[228:231], v[70:73]
	v_mfma_f32_16x16x32_bf16 v[66:69], v[192:195], v[228:231], v[66:69]
	s_setprio 0
	s_barrier
; #define PG8_STAGE(bufoff, gbase, voff) do { _Pragma("unroll") for (int _i = 0; _i < 2; ++_i) \
;         __builtin_amdgcn_global_load_lds((const unsigned*)((const char*)(gbase) + (voff)[_i]), (LAS unsigned*)(lds + (bufoff) + ldsw + _i * 8192), 16, 0, 0); } while (0)
; #define PG8_LDA(dst, b, h) do { _Pragma("unroll") for (int m = 0; m < 4; ++m) _Pragma("unroll") for (int k = 0; k < 2; ++k) dst[m][k] = *(const LAS bf16x8*)(lds + PG8_SA(b, h) + ((aoff ^ (k * 64)) + m * 2048)); } while (0)
; #define PG8_MMA(ai, bj, At, Bt) do { __builtin_amdgcn_s_setprio(1); _Pragma("unroll") for (int m = 0; m < 4; ++m) _Pragma("unroll") for (int n = 0; n < 2; ++n) _Pragma("unroll") for (int k = 0; k < 2; ++k) \
;         acc[ai][bj][m][n] = __builtin_amdgcn_mfma_f32_16x16x32_bf16(Bt[n][k], At[m][k], acc[ai][bj][m][n], 0, 0, 0); __builtin_amdgcn_s_setprio(0); } while (0)
; #define PG8_WAIT_V(n) asm volatile("s_waitcnt vmcnt(" #n ")" ::: "memory")
; #define PG8_WAIT_L(n) asm volatile("s_waitcnt lgkmcnt(" #n ")" ::: "memory")
; #define PG8_BAR __builtin_amdgcn_s_barrier()
; #define PG8_SCHED __builtin_amdgcn_sched_barrier(0)
;     ...
;             PG8_LDA(At, 1, 1); PG8_STAGE(PG8_SB(1, 0), b3, voffB); PG8_STAGE(PG8_SB(1, 1), b3 + hstep, voffB); PG8_STAGE(PG8_SA(1, 0), a3, vs[0]);
;             PG8_WAIT_V(8); PG8_WAIT_L(0); PG8_BAR; if (do1) { PG8_MMA(1, 0, At, B0); PG8_MMA(1, 1, At, B1); } PG8_BAR; PG8_SCHED;
;         }
;         if (wr == 0) PG8_BAR;
	s_add_i32 s26, s57, s30
	v_lshl_add_u64 v[196:197], s[24:25], 0, v[132:133]
	s_mov_b32 m0, s26
	ds_read_b128 v[200:203], v161 offset:49152
	ds_read_b128 v[204:207], v161 offset:51200
	ds_read_b128 v[208:211], v162 offset:49152
	ds_read_b128 v[212:215], v162 offset:51200
	ds_read_b128 v[216:219], v161 offset:53248
	ds_read_b128 v[220:223], v161 offset:55296
	ds_read_b128 v[224:227], v162 offset:53248
	ds_read_b128 v[228:231], v162 offset:55296
	global_load_lds_dwordx4 v[196:197], off
	s_add_i32 m0, s26, 0x2000
	s_add_u32 s22, s22, 0xb4000
	v_lshl_add_u64 v[196:197], s[24:25], 0, v[130:131]
	s_addc_u32 s23, s23, 0
	s_add_i32 s24, s58, s30
	global_load_lds_dwordx4 v[196:197], off
	v_lshl_add_u64 v[196:197], s[22:23], 0, v[132:133]
	s_mov_b32 m0, s24
	s_nop 0
	global_load_lds_dwordx4 v[196:197], off
	v_lshl_add_u64 v[196:197], s[22:23], 0, v[130:131]
	s_add_i32 m0, s24, 0x2000
	s_nop 0
	global_load_lds_dwordx4 v[196:197], off
	v_lshl_add_u64 v[196:197], s[20:21], 0, v[134:135]
	s_mov_b32 m0, s39
	s_nop 0
	global_load_lds_dwordx4 v[196:197], off nt
	v_lshl_add_u64 v[196:197], s[20:21], 0, v[136:137]
	s_mov_b32 m0, s40
	s_nop 0
	global_load_lds_dwordx4 v[196:197], off nt
	s_waitcnt vmcnt(8)
	s_waitcnt lgkmcnt(0)
	s_barrier
	s_setprio 1
	v_mfma_f32_16x16x32_bf16 v[62:65], v[146:149], v[200:203], v[62:65]
	v_mfma_f32_16x16x32_bf16 v[58:61], v[172:175], v[200:203], v[58:61]
	v_mfma_f32_16x16x32_bf16 v[46:49], v[146:149], v[204:207], v[46:49]
	v_mfma_f32_16x16x32_bf16 v[42:45], v[172:175], v[204:207], v[42:45]
	v_mfma_f32_16x16x32_bf16 v[30:33], v[146:149], v[216:219], v[30:33]
	v_mfma_f32_16x16x32_bf16 v[26:29], v[172:175], v[216:219], v[26:29]
	v_mfma_f32_16x16x32_bf16 v[14:17], v[146:149], v[220:223], v[14:17]
	v_mfma_f32_16x16x32_bf16 v[10:13], v[172:175], v[220:223], v[10:13]
	v_mfma_f32_16x16x32_bf16 v[62:65], v[168:171], v[208:211], v[62:65]
	v_mfma_f32_16x16x32_bf16 v[58:61], v[176:179], v[208:211], v[58:61]
	v_mfma_f32_16x16x32_bf16 v[46:49], v[168:171], v[212:215], v[46:49]
	v_mfma_f32_16x16x32_bf16 v[42:45], v[176:179], v[212:215], v[42:45]
	v_mfma_f32_16x16x32_bf16 v[30:33], v[168:171], v[224:227], v[30:33]
	v_mfma_f32_16x16x32_bf16 v[26:29], v[176:179], v[224:227], v[26:29]
	v_mfma_f32_16x16x32_bf16 v[14:17], v[168:171], v[228:231], v[14:17]
	v_mfma_f32_16x16x32_bf16 v[10:13], v[176:179], v[228:231], v[10:13]
	v_mfma_f32_16x16x32_bf16 v[54:57], v[180:183], v[200:203], v[54:57]
	v_mfma_f32_16x16x32_bf16 v[50:53], v[188:191], v[200:203], v[50:53]
	v_mfma_f32_16x16x32_bf16 v[38:41], v[180:183], v[204:207], v[38:41]
	v_mfma_f32_16x16x32_bf16 v[34:37], v[188:191], v[204:207], v[34:37]
	v_mfma_f32_16x16x32_bf16 v[22:25], v[180:183], v[216:219], v[22:25]
	v_mfma_f32_16x16x32_bf16 v[18:21], v[188:191], v[216:219], v[18:21]
	v_mfma_f32_16x16x32_bf16 v[6:9], v[180:183], v[220:223], v[6:9]
	v_mfma_f32_16x16x32_bf16 v[2:5], v[188:191], v[220:223], v[2:5]
	v_mfma_f32_16x16x32_bf16 v[54:57], v[184:187], v[208:211], v[54:57]
	v_mfma_f32_16x16x32_bf16 v[50:53], v[192:195], v[208:211], v[50:53]
	v_mfma_f32_16x16x32_bf16 v[38:41], v[184:187], v[212:215], v[38:41]
	v_mfma_f32_16x16x32_bf16 v[34:37], v[192:195], v[212:215], v[34:37]
	v_mfma_f32_16x16x32_bf16 v[22:25], v[184:187], v[224:227], v[22:25]
	v_mfma_f32_16x16x32_bf16 v[18:21], v[192:195], v[224:227], v[18:21]
	v_mfma_f32_16x16x32_bf16 v[6:9], v[184:187], v[228:231], v[6:9]
	v_mfma_f32_16x16x32_bf16 v[2:5], v[192:195], v[228:231], v[2:5]
	s_setprio 0
	s_barrier
	s_add_i32 s56, s56, 2
	s_add_u32 s18, s18, 0x8000
	s_addc_u32 s19, s19, 0
	s_add_u32 s54, s54, 0x8000
	s_addc_u32 s55, s55, 0
	s_cmp_gt_u32 s56, 41
	s_cbranch_scc0 .LBB0_2411
	s_and_b64 vcc, exec, s[4:5]
	s_cbranch_vccz .LBB0_2414
	s_barrier
